# speedup vs baseline: 1.0150x; 1.0034x over previous
_Z13gemm8p_kernel5GArgs:
	s_add_i32 s3, s2, 0x120
	s_sub_i32 s26, s2, 0xc0
	s_cmp_lt_u32 s2, 0xc0
	s_cselect_b32 s2, s3, s26
	s_load_dwordx4 s[20:23], s[0:1], 0x80
	s_load_dwordx8 s[4:11], s[0:1], 0x0
	s_load_dwordx8 s[12:19], s[0:1], 0x48
	s_load_dwordx2 s[24:25], s[0:1], 0x38
	v_and_b32_e32 v2, 32, v0
	s_waitcnt lgkmcnt(0)
	s_cmp_lt_i32 s2, s22
	s_cselect_b64 s[26:27], -1, 0
	s_and_b64 s[28:29], s[26:27], exec
	s_cselect_b32 s12, s4, s12
	s_cselect_b32 s3, s25, s21
	s_cselect_b32 s4, 0, s22
	s_cselect_b32 s13, s5, s13
	s_cselect_b32 s7, s7, s15
	s_cselect_b32 s14, s6, s14
	s_sub_i32 s2, s2, s4
	s_lshl_b32 s4, s3, 2
	s_lshl_b32 s3, s3, 4
	s_abs_i32 s15, s3
	v_cvt_f32_u32_e32 v1, s15
	s_ashr_i32 s5, s2, 31
	s_lshr_b32 s5, s5, 29
	s_add_i32 s5, s2, s5
	v_rcp_iflag_f32_e32 v1, v1
	s_ashr_i32 s6, s5, 3
	s_and_b32 s5, s5, -8
	s_sub_i32 s2, s2, s5
	v_mul_f32_e32 v1, 0x4f7ffffe, v1
	v_cvt_u32_f32_e32 v1, v1
	s_lshr_b32 s5, s2, 31
	s_or_b32 s4, s5, s4
	s_mul_i32 s2, s4, s2
	s_add_i32 s2, s2, s6
	s_sub_i32 s6, 0, s15
	v_readfirstlane_b32 s21, v1
	s_mul_i32 s6, s6, s21
	s_mul_hi_u32 s6, s21, s6
	s_abs_i32 s5, s2
	s_add_i32 s21, s21, s6
	s_mul_hi_u32 s6, s5, s21
	s_mul_i32 s21, s6, s15
	s_xor_b32 s4, s2, s3
	s_sub_i32 s5, s5, s21
	s_ashr_i32 s4, s4, 31
	s_add_i32 s21, s6, 1
	s_sub_i32 s22, s5, s15
	s_cmp_ge_u32 s5, s15
	s_cselect_b32 s6, s21, s6
	s_cselect_b32 s5, s22, s5
	s_add_i32 s21, s6, 1
	s_cmp_ge_u32 s5, s15
	s_cselect_b32 s5, s21, s6
	s_xor_b32 s5, s5, s4
	s_sub_i32 s4, s5, s4
	s_lshl_b32 s5, s4, 4
	s_sub_i32 s6, 32, s5
	s_min_i32 s6, s6, 16
	s_abs_i32 s15, s6
	v_cvt_f32_u32_e32 v1, s15
	s_sub_i32 s21, 0, s15
	s_mul_i32 s4, s4, s3
	s_sub_i32 s2, s2, s4
	v_rcp_iflag_f32_e32 v1, v1
	s_abs_i32 s4, s2
	s_xor_b32 s3, s2, s6
	s_ashr_i32 s3, s3, 31
	v_mul_f32_e32 v1, 0x4f7ffffe, v1
	v_cvt_u32_f32_e32 v1, v1
	v_bfe_u32 v155, v0, 2, 4
	v_mov_b32_e32 v3, 0
	v_lshrrev_b32_e32 v6, 3, v0
	v_readfirstlane_b32 s22, v1
	s_mul_i32 s21, s21, s22
	s_mul_hi_u32 s21, s22, s21
	s_add_i32 s22, s22, s21
	s_mul_hi_u32 s21, s4, s22
	s_mul_i32 s22, s21, s15
	s_sub_i32 s4, s4, s22
	s_add_i32 s22, s21, 1
	s_sub_i32 s23, s4, s15
	s_cmp_ge_u32 s4, s15
	s_cselect_b32 s21, s22, s21
	s_cselect_b32 s4, s23, s4
	s_add_i32 s22, s21, 1
	s_cmp_ge_u32 s4, s15
	s_cselect_b32 s4, s22, s21
	s_xor_b32 s4, s4, s3
	s_sub_i32 s4, s4, s3
	s_mul_i32 s3, s4, s6
	s_sub_i32 s2, s2, s3
	s_add_i32 s15, s2, s5
	s_lshl_b32 s2, s4, 8
	s_lshl_b32 s6, s15, 8
	s_ashr_i32 s3, s2, 31
	v_lshlrev_b32_e32 v1, 4, v0
	s_mul_i32 s4, s4, 0x30000
	v_bitop3_b32 v2, v1, v2, 48 bitop3:0x6c
	s_mul_hi_i32 s5, s2, 0x300
	s_add_u32 s4, s14, s4
	v_and_or_b32 v2, v0, 64, v2
	s_addc_u32 s5, s7, s5
	v_or_b32_e32 v38, 0x10000, v1
	v_lshl_add_u64 v[4:5], s[4:5], 0, v[2:3]
	v_and_or_b32 v7, v6, 48, v155
	v_readfirstlane_b32 s4, v38
	v_mul_u32_u24_e32 v18, 0x300, v7
	v_mov_b32_e32 v19, v3
	s_mov_b32 m0, s4
	v_or_b32_e32 v6, 64, v6
	s_movk_i32 s4, 0x70
	v_or_b32_e32 v41, 0x12000, v1
	v_lshl_add_u64 v[14:15], v[4:5], 0, v[18:19]
	v_and_or_b32 v6, v6, s4, v155
	v_readfirstlane_b32 s4, v41
	s_mul_i32 s15, s15, 0x30000
	global_load_lds_dwordx4 v[14:15], off
	s_mov_b32 m0, s4
	s_mul_hi_i32 s5, s6, 0x300
	s_add_u32 s4, s12, s15
	v_mul_u32_u24_e32 v20, 0x300, v6
	v_mov_b32_e32 v21, v3
	s_addc_u32 s5, s13, s5
	v_lshl_add_u64 v[16:17], v[4:5], 0, v[20:21]
	v_lshl_add_u64 v[4:5], s[4:5], 0, v[2:3]
	v_readfirstlane_b32 s4, v1
	v_or_b32_e32 v37, 0x2000, v1
	global_load_lds_dwordx4 v[16:17], off
	v_lshl_add_u64 v[10:11], v[4:5], 0, v[18:19]
	s_mov_b32 m0, s4
	v_readfirstlane_b32 s4, v37
	global_load_lds_dwordx4 v[10:11], off
	s_mov_b32 m0, s4
	s_or_b32 s4, s2, 0x80
	s_mul_hi_i32 s5, s4, 0x300
	s_mulk_i32 s4, 0x300
	s_add_u32 s4, s14, s4
	s_addc_u32 s5, s7, s5
	v_or_b32_e32 v35, 0x14000, v1
	v_lshl_add_u64 v[12:13], v[4:5], 0, v[20:21]
	v_lshl_add_u64 v[4:5], s[4:5], 0, v[2:3]
	v_readfirstlane_b32 s4, v35
	v_or_b32_e32 v36, 0x16000, v1
	global_load_lds_dwordx4 v[12:13], off
	v_lshl_add_u64 v[6:7], v[4:5], 0, v[18:19]
	s_mov_b32 m0, s4
	v_readfirstlane_b32 s4, v36
	global_load_lds_dwordx4 v[6:7], off
	s_mov_b32 m0, s4
	s_or_b32 s4, s6, 0x80
	s_mul_hi_i32 s5, s4, 0x300
	s_mulk_i32 s4, 0x300
	s_add_u32 s4, s12, s4
	s_addc_u32 s5, s13, s5
	v_or_b32_e32 v39, 0x4000, v1
	v_lshl_add_u64 v[8:9], v[4:5], 0, v[20:21]
	v_lshl_add_u64 v[4:5], s[4:5], 0, v[2:3]
	v_readfirstlane_b32 s4, v39
	v_or_b32_e32 v40, 0x6000, v1
	global_load_lds_dwordx4 v[8:9], off
	v_lshl_add_u64 v[2:3], v[4:5], 0, v[18:19]
	s_mov_b32 m0, s4
	v_readfirstlane_b32 s4, v40
	global_load_lds_dwordx4 v[2:3], off
	v_lshl_add_u64 v[4:5], v[4:5], 0, v[20:21]
	s_mov_b32 m0, s4
	v_lshrrev_b32_e32 v18, 8, v0
	global_load_lds_dwordx4 v[4:5], off
	v_cmp_eq_u32_e32 vcc, 1, v18
	s_and_saveexec_b64 s[4:5], vcc
	s_cbranch_execz .LBB2_2
	s_barrier
